# peer_up: accumulator-register pick by v_cndmask instead of exec-mask branches; 8 MFMAs back to back; interleaved quad sums (on top of gemm3 L0 epilogue pipelining)
# speedup vs baseline: 1.0171x; 1.0046x over previous
.LBB0_997:
	s_mov_b32 s51, s50
	s_add_i32 s50, s50, s30
	s_min_i32 s14, s50, s5
	s_ashr_i32 s15, s14, 31
	s_lshl_b64 s[16:17], s[14:15], 9
	v_lshl_add_u64 v[70:71], v[148:149], 0, s[16:17]
	s_lshl_b64 s[14:15], s[14:15], 12
	global_load_dwordx2 v[162:163], v[70:71], off
	v_lshl_add_u64 v[70:71], v[156:157], 0, s[14:15]
	v_mov_b32_e32 v134, v182
	global_load_dword v182, v[70:71], off
	s_waitcnt vmcnt(19)
	ds_bpermute_b32 v70, v165, v160
	ds_bpermute_b32 v71, v165, v161
	ds_bpermute_b32 v72, v167, v160
	ds_bpermute_b32 v73, v167, v161
	s_waitcnt lgkmcnt(3)
	v_lshl_or_b32 v70, v70, 7, v164
	s_waitcnt lgkmcnt(2)
	v_lshl_or_b32 v71, v71, 7, v164
	global_load_dwordx4 v[126:129], v70, s[12:13]
	global_load_dwordx4 v[130:133], v71, s[12:13]
	ds_bpermute_b32 v71, v168, v160
	s_waitcnt lgkmcnt(2)
	v_lshl_or_b32 v70, v72, 7, v164
	s_waitcnt lgkmcnt(1)
	v_lshl_or_b32 v72, v73, 7, v164
	ds_bpermute_b32 v73, v168, v161
	global_load_dwordx4 v[118:121], v70, s[12:13]
	global_load_dwordx4 v[122:125], v72, s[12:13]
	s_waitcnt lgkmcnt(1)
	v_lshl_or_b32 v70, v71, 7, v164
	ds_bpermute_b32 v71, v169, v160
	s_waitcnt lgkmcnt(1)
	v_lshl_or_b32 v72, v73, 7, v164
	ds_bpermute_b32 v73, v169, v161
	global_load_dwordx4 v[110:113], v70, s[12:13]
	global_load_dwordx4 v[114:117], v72, s[12:13]
	s_waitcnt lgkmcnt(1)
	v_lshl_or_b32 v70, v71, 7, v164
	ds_bpermute_b32 v71, v170, v160
	s_waitcnt lgkmcnt(1)
	v_lshl_or_b32 v72, v73, 7, v164
	ds_bpermute_b32 v73, v170, v161
	global_load_dwordx4 v[102:105], v70, s[12:13]
	global_load_dwordx4 v[106:109], v72, s[12:13]
	s_waitcnt lgkmcnt(1)
	v_lshl_or_b32 v70, v71, 7, v164
	ds_bpermute_b32 v71, v171, v160
	s_waitcnt lgkmcnt(1)
	v_lshl_or_b32 v72, v73, 7, v164
	ds_bpermute_b32 v73, v171, v161
	global_load_dwordx4 v[94:97], v70, s[12:13]
	global_load_dwordx4 v[98:101], v72, s[12:13]
	s_waitcnt lgkmcnt(1)
	v_lshl_or_b32 v70, v71, 7, v164
	ds_bpermute_b32 v71, v172, v160
	s_waitcnt lgkmcnt(1)
	v_lshl_or_b32 v72, v73, 7, v164
	ds_bpermute_b32 v73, v172, v161
	global_load_dwordx4 v[86:89], v70, s[12:13]
	global_load_dwordx4 v[90:93], v72, s[12:13]
	s_waitcnt lgkmcnt(1)
	v_lshl_or_b32 v70, v71, 7, v164
	ds_bpermute_b32 v71, v173, v160
	ds_bpermute_b32 v72, v173, v161
	s_waitcnt lgkmcnt(2)
	v_lshl_or_b32 v73, v73, 7, v164
	global_load_dwordx4 v[78:81], v70, s[12:13]
	global_load_dwordx4 v[82:85], v73, s[12:13]
	s_waitcnt lgkmcnt(1)
	v_lshl_or_b32 v70, v71, 7, v164
	s_waitcnt lgkmcnt(0)
	v_lshl_or_b32 v74, v72, 7, v164
	global_load_dwordx4 v[70:73], v70, s[12:13]
	s_nop 0
	global_load_dwordx4 v[74:77], v74, s[12:13]
	ds_bpermute_b32 v135, v166, v134
	ds_bpermute_b32 v136, v175, v134
	v_mov_b32_e32 v137, v4
	ds_bpermute_b32 v138, v176, v134
	ds_bpermute_b32 v141, v180, v134
	s_waitcnt lgkmcnt(3)
	v_lshlrev_b32_e32 v139, 16, v135
	v_and_b32_e32 v135, 0xffff0000, v135
	v_cvt_pk_fp8_f32 v137, v139, v135
	ds_bpermute_b32 v135, v177, v134
	s_waitcnt lgkmcnt(3)
	v_lshlrev_b32_e32 v139, 16, v136
	v_and_b32_e32 v136, 0xffff0000, v136
	v_cvt_pk_fp8_f32 v137, v139, v136 op_sel:[0,0,1]
	s_waitcnt lgkmcnt(2)
	v_lshlrev_b32_e32 v136, 16, v138
	v_and_b32_e32 v138, 0xffff0000, v138
	v_mov_b32_e32 v139, v4
	v_cvt_pk_fp8_f32 v139, v136, v138
	ds_bpermute_b32 v136, v178, v134
	s_waitcnt lgkmcnt(1)
	v_lshlrev_b32_e32 v138, 16, v135
	v_and_b32_e32 v135, 0xffff0000, v135
	v_cvt_pk_fp8_f32 v139, v138, v135 op_sel:[0,0,1]
	ds_bpermute_b32 v135, v179, v134
	s_waitcnt lgkmcnt(1)
	v_lshlrev_b32_e32 v138, 16, v136
	v_and_b32_e32 v136, 0xffff0000, v136
	v_mov_b32_e32 v140, v4
	ds_bpermute_b32 v134, v181, v134
	v_cvt_pk_fp8_f32 v140, v138, v136
	v_lshlrev_b32_e32 v138, 16, v141
	v_and_b32_e32 v141, 0xffff0000, v141
	v_mov_b32_e32 v160, v4
	v_cvt_pk_fp8_f32 v160, v138, v141
	s_waitcnt lgkmcnt(1)
	v_lshlrev_b32_e32 v136, 16, v135
	v_and_b32_e32 v135, 0xffff0000, v135
	v_cvt_pk_fp8_f32 v140, v136, v135 op_sel:[0,0,1]
	s_waitcnt lgkmcnt(0)
	v_lshlrev_b32_e32 v135, 16, v134
	v_and_b32_e32 v134, 0xffff0000, v134
	v_cvt_pk_fp8_f32 v160, v135, v134 op_sel:[0,0,1]
	v_cndmask_b32_e64 v135, 0, v137, s[38:39]
	v_cndmask_b32_e64 v136, 0, v139, s[38:39]
	v_cndmask_b32_e64 v137, 0, v140, s[38:39]
	v_cndmask_b32_e64 v141, 0, v160, s[38:39]
	v_cndmask_b32_e64 v134, 0, v135, s[40:41]
	v_cndmask_b32_e64 v138, v135, 0, s[40:41]
	v_cndmask_b32_e64 v135, 0, v136, s[40:41]
	v_cndmask_b32_e64 v139, v136, 0, s[40:41]
	v_cndmask_b32_e64 v136, 0, v137, s[40:41]
	v_cndmask_b32_e64 v140, v137, 0, s[40:41]
	v_cndmask_b32_e64 v137, 0, v141, s[40:41]
	v_cndmask_b32_e64 v141, v141, 0, s[40:41]
	s_waitcnt vmcnt(34)
	v_mov_b32_e32 v184, v183
	v_cmp_lt_i32_e32 vcc, 0, v5
	s_waitcnt vmcnt(18)
	v_mfma_scale_f32_16x16x128_f8f6f4 v[62:65], v[62:69], v[134:141], 0, v1, v1 op_sel_hi:[0,0,0]
	v_mfma_scale_f32_16x16x128_f8f6f4 v[54:57], v[54:61], v[134:141], 0, v1, v1 op_sel_hi:[0,0,0]
	v_mfma_scale_f32_16x16x128_f8f6f4 v[46:49], v[46:53], v[134:141], 0, v1, v1 op_sel_hi:[0,0,0]
	v_mfma_scale_f32_16x16x128_f8f6f4 v[38:41], v[38:45], v[134:141], 0, v1, v1 op_sel_hi:[0,0,0]
	v_mfma_scale_f32_16x16x128_f8f6f4 v[30:33], v[30:37], v[134:141], 0, v1, v1 op_sel_hi:[0,0,0]
	v_mfma_scale_f32_16x16x128_f8f6f4 v[22:25], v[22:29], v[134:141], 0, v1, v1 op_sel_hi:[0,0,0]
	v_mfma_scale_f32_16x16x128_f8f6f4 v[14:17], v[14:21], v[134:141], 0, v1, v1 op_sel_hi:[0,0,0]
	v_mfma_scale_f32_16x16x128_f8f6f4 v[6:9], v[6:13], v[134:141], 0, v1, v1 op_sel_hi:[0,0,0]
	s_nop 5
	v_cndmask_b32_e64 v64, v65, v64, s[42:43]
	v_cndmask_b32_e64 v63, v63, v64, s[48:49]
	v_cndmask_b32_e64 v62, v62, v63, s[46:47]
	v_cndmask_b32_e64 v56, v57, v56, s[42:43]
	v_cndmask_b32_e64 v55, v55, v56, s[48:49]
	v_cndmask_b32_e64 v54, v54, v55, s[46:47]
	v_cndmask_b32_e64 v48, v49, v48, s[42:43]
	v_cndmask_b32_e64 v47, v47, v48, s[48:49]
	v_cndmask_b32_e64 v46, v46, v47, s[46:47]
	v_cndmask_b32_e64 v40, v41, v40, s[42:43]
	v_cndmask_b32_e64 v39, v39, v40, s[48:49]
	v_cndmask_b32_e64 v38, v38, v39, s[46:47]
	v_cndmask_b32_e64 v32, v33, v32, s[42:43]
	v_cndmask_b32_e64 v31, v31, v32, s[48:49]
	v_cndmask_b32_e64 v30, v30, v31, s[46:47]
	v_cndmask_b32_e64 v24, v25, v24, s[42:43]
	v_cndmask_b32_e64 v23, v23, v24, s[48:49]
	v_cndmask_b32_e64 v22, v22, v23, s[46:47]
	v_cndmask_b32_e64 v16, v17, v16, s[42:43]
	v_cndmask_b32_e64 v15, v15, v16, s[48:49]
	v_cndmask_b32_e64 v14, v14, v15, s[46:47]
	v_cndmask_b32_e64 v8, v9, v8, s[42:43]
	v_cndmask_b32_e64 v7, v7, v8, s[48:49]
	v_cndmask_b32_e64 v6, v6, v7, s[46:47]
	s_nop 0
	v_add_f32_dpp v62, v62, v62 quad_perm:[1,0,3,2] row_mask:0xf bank_mask:0xf bound_ctrl:1
	v_add_f32_dpp v54, v54, v54 quad_perm:[1,0,3,2] row_mask:0xf bank_mask:0xf bound_ctrl:1
	v_add_f32_dpp v46, v46, v46 quad_perm:[1,0,3,2] row_mask:0xf bank_mask:0xf bound_ctrl:1
	v_add_f32_dpp v38, v38, v38 quad_perm:[1,0,3,2] row_mask:0xf bank_mask:0xf bound_ctrl:1
	v_add_f32_dpp v30, v30, v30 quad_perm:[1,0,3,2] row_mask:0xf bank_mask:0xf bound_ctrl:1
	v_add_f32_dpp v22, v22, v22 quad_perm:[1,0,3,2] row_mask:0xf bank_mask:0xf bound_ctrl:1
	v_add_f32_dpp v14, v14, v14 quad_perm:[1,0,3,2] row_mask:0xf bank_mask:0xf bound_ctrl:1
	v_add_f32_dpp v6, v6, v6 quad_perm:[1,0,3,2] row_mask:0xf bank_mask:0xf bound_ctrl:1
	v_mov_b32_dpp v63, v62 quad_perm:[2,3,0,1] row_mask:0xf bank_mask:0xf bound_ctrl:1
	v_mov_b32_dpp v55, v54 quad_perm:[2,3,0,1] row_mask:0xf bank_mask:0xf bound_ctrl:1
	v_mov_b32_dpp v47, v46 quad_perm:[2,3,0,1] row_mask:0xf bank_mask:0xf bound_ctrl:1
	v_mov_b32_dpp v39, v38 quad_perm:[2,3,0,1] row_mask:0xf bank_mask:0xf bound_ctrl:1
	v_mov_b32_dpp v31, v30 quad_perm:[2,3,0,1] row_mask:0xf bank_mask:0xf bound_ctrl:1
	v_mov_b32_dpp v23, v22 quad_perm:[2,3,0,1] row_mask:0xf bank_mask:0xf bound_ctrl:1
	v_mov_b32_dpp v15, v14 quad_perm:[2,3,0,1] row_mask:0xf bank_mask:0xf bound_ctrl:1
	v_mov_b32_dpp v7, v6 quad_perm:[2,3,0,1] row_mask:0xf bank_mask:0xf bound_ctrl:1
	s_and_saveexec_b64 s[14:15], s[44:45]
	s_cbranch_execz .LBB0_1031
	v_add_f32_e32 v9, v14, v15
	v_add_f32_e32 v8, v22, v23
	v_add_f32_e32 v10, v30, v31
	v_add_f32_e32 v11, v38, v39
	v_add_f32_e32 v12, v46, v47
	v_add_f32_e32 v13, v54, v55
	v_add_f32_e32 v14, v62, v63
	v_add_f32_e32 v15, v6, v7
	v_cvt_pk_bf16_f32 v6, v14, v13
	v_cvt_pk_bf16_f32 v7, v12, v11
	v_cvt_pk_bf16_f32 v8, v10, v8
	v_cvt_pk_bf16_f32 v9, v9, v15
	global_store_dwordx4 v[158:159], v[6:9], off
.LBB0_1031:
	s_or_b64 exec, exec, s[14:15]
	s_add_i32 s14, s33, s51
	s_min_i32 s14, s14, s5
	s_ashr_i32 s15, s14, 31
	s_lshl_b64 s[16:17], s[14:15], 9
	v_lshl_add_u64 v[6:7], v[148:149], 0, s[16:17]
	s_lshl_b64 s[14:15], s[14:15], 12
	global_load_dwordx2 v[160:161], v[6:7], off
	v_lshl_add_u64 v[6:7], v[156:157], 0, s[14:15]
	global_load_dword v183, v[6:7], off
	s_waitcnt vmcnt(19)
	ds_bpermute_b32 v6, v165, v162
	ds_bpermute_b32 v7, v165, v163
	ds_bpermute_b32 v8, v167, v162
	ds_bpermute_b32 v9, v167, v163
	s_waitcnt lgkmcnt(3)
	v_lshl_or_b32 v6, v6, 7, v164
	s_waitcnt lgkmcnt(2)
	v_lshl_or_b32 v7, v7, 7, v164
	global_load_dwordx4 v[62:65], v6, s[12:13]
	global_load_dwordx4 v[66:69], v7, s[12:13]
	ds_bpermute_b32 v7, v168, v162
	s_waitcnt lgkmcnt(2)
	v_lshl_or_b32 v6, v8, 7, v164
	s_waitcnt lgkmcnt(1)
	v_lshl_or_b32 v8, v9, 7, v164
	ds_bpermute_b32 v9, v168, v163
	global_load_dwordx4 v[54:57], v6, s[12:13]
	global_load_dwordx4 v[58:61], v8, s[12:13]
	s_waitcnt lgkmcnt(1)
	v_lshl_or_b32 v6, v7, 7, v164
	ds_bpermute_b32 v7, v169, v162
	s_waitcnt lgkmcnt(1)
	v_lshl_or_b32 v8, v9, 7, v164
	ds_bpermute_b32 v9, v169, v163
	global_load_dwordx4 v[46:49], v6, s[12:13]
	global_load_dwordx4 v[50:53], v8, s[12:13]
	s_waitcnt lgkmcnt(1)
	v_lshl_or_b32 v6, v7, 7, v164
	ds_bpermute_b32 v7, v170, v162
	s_waitcnt lgkmcnt(1)
	v_lshl_or_b32 v8, v9, 7, v164
	ds_bpermute_b32 v9, v170, v163
	global_load_dwordx4 v[38:41], v6, s[12:13]
	global_load_dwordx4 v[42:45], v8, s[12:13]
	s_waitcnt lgkmcnt(1)
	v_lshl_or_b32 v6, v7, 7, v164
	ds_bpermute_b32 v7, v171, v162
	s_waitcnt lgkmcnt(1)
	v_lshl_or_b32 v8, v9, 7, v164
	ds_bpermute_b32 v9, v171, v163
	global_load_dwordx4 v[30:33], v6, s[12:13]
	global_load_dwordx4 v[34:37], v8, s[12:13]
	s_waitcnt lgkmcnt(1)
	v_lshl_or_b32 v6, v7, 7, v164
	ds_bpermute_b32 v7, v172, v162
	s_waitcnt lgkmcnt(1)
	v_lshl_or_b32 v8, v9, 7, v164
	ds_bpermute_b32 v9, v172, v163
	global_load_dwordx4 v[22:25], v6, s[12:13]
	global_load_dwordx4 v[26:29], v8, s[12:13]
	s_waitcnt lgkmcnt(1)
	v_lshl_or_b32 v6, v7, 7, v164
	ds_bpermute_b32 v7, v173, v162
	ds_bpermute_b32 v8, v173, v163
	s_waitcnt lgkmcnt(2)
	v_lshl_or_b32 v9, v9, 7, v164
	global_load_dwordx4 v[14:17], v6, s[12:13]
	global_load_dwordx4 v[18:21], v9, s[12:13]
	s_waitcnt lgkmcnt(1)
	v_lshl_or_b32 v6, v7, 7, v164
	s_waitcnt lgkmcnt(0)
	v_lshl_or_b32 v10, v8, 7, v164
	global_load_dwordx4 v[6:9], v6, s[12:13]
	s_nop 0
	global_load_dwordx4 v[10:13], v10, s[12:13]
	ds_bpermute_b32 v134, v166, v184
	ds_bpermute_b32 v135, v175, v184
	v_mov_b32_e32 v136, 0
	ds_bpermute_b32 v137, v176, v184
	ds_bpermute_b32 v140, v180, v184
	s_waitcnt lgkmcnt(3)
	v_lshlrev_b32_e32 v138, 16, v134
	v_and_b32_e32 v134, 0xffff0000, v134
	v_cvt_pk_fp8_f32 v136, v138, v134
	s_waitcnt lgkmcnt(2)
	v_lshlrev_b32_e32 v138, 16, v135
	v_and_b32_e32 v135, 0xffff0000, v135
	ds_bpermute_b32 v134, v177, v184
	v_cvt_pk_fp8_f32 v136, v138, v135 op_sel:[0,0,1]
	s_waitcnt lgkmcnt(2)
	v_lshlrev_b32_e32 v135, 16, v137
	v_and_b32_e32 v137, 0xffff0000, v137
	v_mov_b32_e32 v138, 0
	v_cvt_pk_fp8_f32 v138, v135, v137
	ds_bpermute_b32 v135, v178, v184
	s_waitcnt lgkmcnt(1)
	v_lshlrev_b32_e32 v137, 16, v134
	v_and_b32_e32 v134, 0xffff0000, v134
	v_cvt_pk_fp8_f32 v138, v137, v134 op_sel:[0,0,1]
	ds_bpermute_b32 v134, v179, v184
	s_waitcnt lgkmcnt(1)
	v_lshlrev_b32_e32 v137, 16, v135
	v_and_b32_e32 v135, 0xffff0000, v135
	v_mov_b32_e32 v139, 0
	v_cvt_pk_fp8_f32 v139, v137, v135
	ds_bpermute_b32 v137, v181, v184
	v_lshlrev_b32_e32 v141, 16, v140
	v_and_b32_e32 v140, 0xffff0000, v140
	v_mov_b32_e32 v162, 0
	v_cvt_pk_fp8_f32 v162, v141, v140
	s_waitcnt lgkmcnt(1)
	v_lshlrev_b32_e32 v135, 16, v134
	v_and_b32_e32 v134, 0xffff0000, v134
	v_cvt_pk_fp8_f32 v139, v135, v134 op_sel:[0,0,1]
	s_waitcnt lgkmcnt(0)
	v_lshlrev_b32_e32 v134, 16, v137
	v_and_b32_e32 v135, 0xffff0000, v137
	v_cvt_pk_fp8_f32 v162, v134, v135 op_sel:[0,0,1]
	v_cndmask_b32_e64 v135, 0, v136, s[38:39]
	v_cndmask_b32_e64 v136, 0, v138, s[38:39]
	v_cndmask_b32_e64 v137, 0, v139, s[38:39]
	v_cndmask_b32_e64 v141, 0, v162, s[38:39]
	v_cndmask_b32_e64 v134, 0, v135, s[40:41]
	v_cndmask_b32_e64 v138, v135, 0, s[40:41]
	v_cndmask_b32_e64 v135, 0, v136, s[40:41]
	v_cndmask_b32_e64 v139, v136, 0, s[40:41]
	v_cndmask_b32_e64 v136, 0, v137, s[40:41]
	v_cndmask_b32_e64 v140, v137, 0, s[40:41]
	v_cndmask_b32_e64 v137, 0, v141, s[40:41]
	v_cndmask_b32_e64 v141, v141, 0, s[40:41]
	s_waitcnt vmcnt(32)
	s_nop 0
	v_mfma_scale_f32_16x16x128_f8f6f4 v[126:129], v[126:133], v[134:141], 0, v1, v1 op_sel_hi:[0,0,0]
	s_waitcnt vmcnt(30)
	v_mfma_scale_f32_16x16x128_f8f6f4 v[118:121], v[118:125], v[134:141], 0, v1, v1 op_sel_hi:[0,0,0]
	s_waitcnt vmcnt(28)
	v_mfma_scale_f32_16x16x128_f8f6f4 v[110:113], v[110:117], v[134:141], 0, v1, v1 op_sel_hi:[0,0,0]
	s_waitcnt vmcnt(26)
	v_mfma_scale_f32_16x16x128_f8f6f4 v[102:105], v[102:109], v[134:141], 0, v1, v1 op_sel_hi:[0,0,0]
	s_waitcnt vmcnt(24)
	v_mfma_scale_f32_16x16x128_f8f6f4 v[94:97], v[94:101], v[134:141], 0, v1, v1 op_sel_hi:[0,0,0]
	s_waitcnt vmcnt(22)
	v_mfma_scale_f32_16x16x128_f8f6f4 v[86:89], v[86:93], v[134:141], 0, v1, v1 op_sel_hi:[0,0,0]
	s_waitcnt vmcnt(20)
	v_mfma_scale_f32_16x16x128_f8f6f4 v[78:81], v[78:85], v[134:141], 0, v1, v1 op_sel_hi:[0,0,0]
	s_waitcnt vmcnt(18)
	v_mfma_scale_f32_16x16x128_f8f6f4 v[70:73], v[70:77], v[134:141], 0, v1, v1 op_sel_hi:[0,0,0]
	s_nop 5
	v_cndmask_b32_e64 v128, v129, v128, s[42:43]
	v_cndmask_b32_e64 v127, v127, v128, s[48:49]
	v_cndmask_b32_e64 v126, v126, v127, s[46:47]
	v_cndmask_b32_e64 v120, v121, v120, s[42:43]
	v_cndmask_b32_e64 v119, v119, v120, s[48:49]
	v_cndmask_b32_e64 v118, v118, v119, s[46:47]
	v_cndmask_b32_e64 v112, v113, v112, s[42:43]
	v_cndmask_b32_e64 v111, v111, v112, s[48:49]
	v_cndmask_b32_e64 v110, v110, v111, s[46:47]
	v_cndmask_b32_e64 v104, v105, v104, s[42:43]
	v_cndmask_b32_e64 v103, v103, v104, s[48:49]
	v_cndmask_b32_e64 v102, v102, v103, s[46:47]
	v_cndmask_b32_e64 v96, v97, v96, s[42:43]
	v_cndmask_b32_e64 v95, v95, v96, s[48:49]
	v_cndmask_b32_e64 v94, v94, v95, s[46:47]
	v_cndmask_b32_e64 v88, v89, v88, s[42:43]
	v_cndmask_b32_e64 v87, v87, v88, s[48:49]
	v_cndmask_b32_e64 v86, v86, v87, s[46:47]
	v_cndmask_b32_e64 v80, v81, v80, s[42:43]
	v_cndmask_b32_e64 v79, v79, v80, s[48:49]
	v_cndmask_b32_e64 v78, v78, v79, s[46:47]
	v_cndmask_b32_e64 v72, v73, v72, s[42:43]
	v_cndmask_b32_e64 v71, v71, v72, s[48:49]
	v_cndmask_b32_e64 v70, v70, v71, s[46:47]
	s_nop 0
	v_add_f32_dpp v126, v126, v126 quad_perm:[1,0,3,2] row_mask:0xf bank_mask:0xf bound_ctrl:1
	v_add_f32_dpp v118, v118, v118 quad_perm:[1,0,3,2] row_mask:0xf bank_mask:0xf bound_ctrl:1
	v_add_f32_dpp v110, v110, v110 quad_perm:[1,0,3,2] row_mask:0xf bank_mask:0xf bound_ctrl:1
	v_add_f32_dpp v102, v102, v102 quad_perm:[1,0,3,2] row_mask:0xf bank_mask:0xf bound_ctrl:1
	v_add_f32_dpp v94, v94, v94 quad_perm:[1,0,3,2] row_mask:0xf bank_mask:0xf bound_ctrl:1
	v_add_f32_dpp v86, v86, v86 quad_perm:[1,0,3,2] row_mask:0xf bank_mask:0xf bound_ctrl:1
	v_add_f32_dpp v78, v78, v78 quad_perm:[1,0,3,2] row_mask:0xf bank_mask:0xf bound_ctrl:1
	v_add_f32_dpp v70, v70, v70 quad_perm:[1,0,3,2] row_mask:0xf bank_mask:0xf bound_ctrl:1
	v_mov_b32_dpp v127, v126 quad_perm:[2,3,0,1] row_mask:0xf bank_mask:0xf bound_ctrl:1
	v_mov_b32_dpp v119, v118 quad_perm:[2,3,0,1] row_mask:0xf bank_mask:0xf bound_ctrl:1
	v_mov_b32_dpp v111, v110 quad_perm:[2,3,0,1] row_mask:0xf bank_mask:0xf bound_ctrl:1
	v_mov_b32_dpp v103, v102 quad_perm:[2,3,0,1] row_mask:0xf bank_mask:0xf bound_ctrl:1
	v_mov_b32_dpp v95, v94 quad_perm:[2,3,0,1] row_mask:0xf bank_mask:0xf bound_ctrl:1
	v_mov_b32_dpp v87, v86 quad_perm:[2,3,0,1] row_mask:0xf bank_mask:0xf bound_ctrl:1
	v_mov_b32_dpp v79, v78 quad_perm:[2,3,0,1] row_mask:0xf bank_mask:0xf bound_ctrl:1
	v_mov_b32_dpp v71, v70 quad_perm:[2,3,0,1] row_mask:0xf bank_mask:0xf bound_ctrl:1
	s_add_i32 s16, s28, s51
	s_cmp_lt_i32 s16, s96
	s_cselect_b64 s[14:15], -1, 0
	s_and_b64 s[52:53], s[44:45], s[14:15]
	s_and_saveexec_b64 s[14:15], s[52:53]
	s_cbranch_execz .LBB0_996
	s_ashr_i32 s17, s16, 31
	s_add_u32 s16, s7, s16
	s_addc_u32 s17, 0, s17
	v_add_f32_e32 v72, v86, v87
	v_add_f32_e32 v74, v94, v95
	v_add_f32_e32 v75, v102, v103
	s_lshl_b64 s[16:17], s[16:17], 8
	v_add_f32_e32 v73, v78, v79
	v_add_f32_e32 v76, v110, v111
	v_add_f32_e32 v77, v118, v119
	v_add_f32_e32 v78, v126, v127
	v_add_f32_e32 v79, v70, v71
	v_cvt_pk_bf16_f32 v70, v78, v77
	v_cvt_pk_bf16_f32 v71, v76, v75
	v_cvt_pk_bf16_f32 v72, v74, v72
	v_lshl_add_u64 v[74:75], v[152:153], 0, s[16:17]
	v_cvt_pk_bf16_f32 v73, v73, v79
	global_store_dwordx4 v[74:75], v[70:73], off
	s_branch .LBB0_996
